# attention block seams: the two dword loads of each next-block pointer issued together behind one wait (were two serialized vmcnt(0) round trips), on top of the Q-in-registers version
# speedup vs baseline: 1.0048x; 1.0048x over previous
.Lstg_b8:
	v_mov_b64_e32 v[144:145], s[70:71]
	flat_load_dword v146, v[144:145] sc0 sc1
	v_mov_b64_e32 v[144:145], s[76:77]
	flat_load_dword v144, v[144:145] sc0 sc1
	s_waitcnt vmcnt(0) lgkmcnt(0)
	v_readfirstlane_b32 s6, v146
	v_readfirstlane_b32 s7, v144
	s_nop 1
	s_nop 3
	s_mov_b32 m0, s81
	s_nop 0
	global_load_lds_dwordx4 v162, s[6:7]
	s_nop 3
	s_add_i32 m0, s78, 0xffffff80
	s_nop 0
	global_load_lds_dwordx4 v162, s[6:7] offset:128
	s_add_i32 m0, s69, 0xffffff00
	s_nop 0
	global_load_lds_dwordx4 v162, s[6:7] offset:256
	s_add_i32 m0, s68, 0xfffffe80
	s_nop 0
	global_load_lds_dwordx4 v162, s[6:7] offset:384
	ds_read_b64_tr_b16 v[144:145], v177 offset:0x8000
	ds_read_b64_tr_b16 v[146:147], v177 offset:0x9000
	ds_read_b64_tr_b16 v[148:149], v177 offset:0xa000
	ds_read_b64_tr_b16 v[150:151], v177 offset:0xb000
	ds_read_b64_tr_b16 v[152:153], v177 offset:0xc000
	ds_read_b64_tr_b16 v[154:155], v177 offset:0xd000
	ds_read_b64_tr_b16 v[156:157], v177 offset:0xe000
	ds_read_b64_tr_b16 v[158:159], v177 offset:0xf000
	ds_read_b64_tr_b16 v[166:167], v177 offset:0x8200
	ds_read_b64_tr_b16 v[168:169], v177 offset:0x9200
	ds_read_b64_tr_b16 v[170:171], v177 offset:0xa200
	ds_read_b64_tr_b16 v[172:173], v177 offset:0xb200
	ds_read_b64_tr_b16 v[180:181], v177 offset:0xc200
	ds_read_b64_tr_b16 v[182:183], v177 offset:0xd200
	ds_read_b64_tr_b16 v[184:185], v177 offset:0xe200
	ds_read_b64_tr_b16 v[186:187], v177 offset:0xf200
	s_waitcnt lgkmcnt(8)
	s_nop 1
	v_mfma_f32_32x32x16_bf16 v[112:127], v[144:147], v[128:131], v[112:127]
	v_mfma_f32_32x32x16_bf16 v[112:127], v[148:151], v[132:135], v[112:127]
	v_mfma_f32_32x32x16_bf16 v[112:127], v[152:155], v[136:139], v[112:127]
	v_mfma_f32_32x32x16_bf16 v[112:127], v[156:159], v[140:143], v[112:127]
	ds_read_b64_tr_b16 v[144:145], v177 offset:0x8400
	ds_read_b64_tr_b16 v[146:147], v177 offset:0x9400
	ds_read_b64_tr_b16 v[148:149], v177 offset:0xa400
	ds_read_b64_tr_b16 v[150:151], v177 offset:0xb400
	ds_read_b64_tr_b16 v[152:153], v177 offset:0xc400
	ds_read_b64_tr_b16 v[154:155], v177 offset:0xd400
	ds_read_b64_tr_b16 v[156:157], v177 offset:0xe400
	ds_read_b64_tr_b16 v[158:159], v177 offset:0xf400
	s_waitcnt lgkmcnt(8)
	v_mfma_f32_32x32x16_bf16 v[0:15], v[166:169], v[128:131], v[0:15]
	v_mfma_f32_32x32x16_bf16 v[0:15], v[170:173], v[132:135], v[0:15]
	v_mfma_f32_32x32x16_bf16 v[0:15], v[180:183], v[136:139], v[0:15]
	v_mfma_f32_32x32x16_bf16 v[0:15], v[184:187], v[140:143], v[0:15]
	ds_read_b64_tr_b16 v[166:167], v177 offset:0x8600
	ds_read_b64_tr_b16 v[168:169], v177 offset:0x9600
	ds_read_b64_tr_b16 v[170:171], v177 offset:0xa600
	ds_read_b64_tr_b16 v[172:173], v177 offset:0xb600
	ds_read_b64_tr_b16 v[180:181], v177 offset:0xc600
	ds_read_b64_tr_b16 v[182:183], v177 offset:0xd600
	ds_read_b64_tr_b16 v[184:185], v177 offset:0xe600
	ds_read_b64_tr_b16 v[186:187], v177 offset:0xf600
	s_waitcnt lgkmcnt(8)
	v_mfma_f32_32x32x16_bf16 v[16:31], v[144:147], v[128:131], v[16:31]
	v_mfma_f32_32x32x16_bf16 v[16:31], v[148:151], v[132:135], v[16:31]
	v_mfma_f32_32x32x16_bf16 v[16:31], v[152:155], v[136:139], v[16:31]
	v_mfma_f32_32x32x16_bf16 v[16:31], v[156:159], v[140:143], v[16:31]
	ds_read_b64_tr_b16 v[144:145], v177 offset:0x8800
	ds_read_b64_tr_b16 v[146:147], v177 offset:0x9800
	ds_read_b64_tr_b16 v[148:149], v177 offset:0xa800
	ds_read_b64_tr_b16 v[150:151], v177 offset:0xb800
	ds_read_b64_tr_b16 v[152:153], v177 offset:0xc800
	ds_read_b64_tr_b16 v[154:155], v177 offset:0xd800
	ds_read_b64_tr_b16 v[156:157], v177 offset:0xe800
	ds_read_b64_tr_b16 v[158:159], v177 offset:0xf800
	s_waitcnt lgkmcnt(8)
	v_mfma_f32_32x32x16_bf16 v[32:47], v[166:169], v[128:131], v[32:47]
	v_mfma_f32_32x32x16_bf16 v[32:47], v[170:173], v[132:135], v[32:47]
	v_mfma_f32_32x32x16_bf16 v[32:47], v[180:183], v[136:139], v[32:47]
	v_mfma_f32_32x32x16_bf16 v[32:47], v[184:187], v[140:143], v[32:47]
	ds_read_b64_tr_b16 v[166:167], v177 offset:0x8a00
	ds_read_b64_tr_b16 v[168:169], v177 offset:0x9a00
	ds_read_b64_tr_b16 v[170:171], v177 offset:0xaa00
	ds_read_b64_tr_b16 v[172:173], v177 offset:0xba00
	ds_read_b64_tr_b16 v[180:181], v177 offset:0xca00
	ds_read_b64_tr_b16 v[182:183], v177 offset:0xda00
	ds_read_b64_tr_b16 v[184:185], v177 offset:0xea00
	ds_read_b64_tr_b16 v[186:187], v177 offset:0xfa00
	s_waitcnt lgkmcnt(8)
	v_mfma_f32_32x32x16_bf16 v[48:63], v[144:147], v[128:131], v[48:63]
	v_mfma_f32_32x32x16_bf16 v[48:63], v[148:151], v[132:135], v[48:63]
	v_mfma_f32_32x32x16_bf16 v[48:63], v[152:155], v[136:139], v[48:63]
	v_mfma_f32_32x32x16_bf16 v[48:63], v[156:159], v[140:143], v[48:63]
	ds_read_b64_tr_b16 v[144:145], v177 offset:0x8c00
	ds_read_b64_tr_b16 v[146:147], v177 offset:0x9c00
	ds_read_b64_tr_b16 v[148:149], v177 offset:0xac00
	ds_read_b64_tr_b16 v[150:151], v177 offset:0xbc00
	ds_read_b64_tr_b16 v[152:153], v177 offset:0xcc00
	ds_read_b64_tr_b16 v[154:155], v177 offset:0xdc00
	ds_read_b64_tr_b16 v[156:157], v177 offset:0xec00
	ds_read_b64_tr_b16 v[158:159], v177 offset:0xfc00
	s_waitcnt lgkmcnt(8)
	v_mfma_f32_32x32x16_bf16 v[64:79], v[166:169], v[128:131], v[64:79]
	v_mfma_f32_32x32x16_bf16 v[64:79], v[170:173], v[132:135], v[64:79]
	v_mfma_f32_32x32x16_bf16 v[64:79], v[180:183], v[136:139], v[64:79]
	v_mfma_f32_32x32x16_bf16 v[64:79], v[184:187], v[140:143], v[64:79]
	ds_read_b64_tr_b16 v[166:167], v177 offset:0x8e00
	ds_read_b64_tr_b16 v[168:169], v177 offset:0x9e00
	ds_read_b64_tr_b16 v[170:171], v177 offset:0xae00
	ds_read_b64_tr_b16 v[172:173], v177 offset:0xbe00
	ds_read_b64_tr_b16 v[180:181], v177 offset:0xce00
	ds_read_b64_tr_b16 v[182:183], v177 offset:0xde00
	ds_read_b64_tr_b16 v[184:185], v177 offset:0xee00
	ds_read_b64_tr_b16 v[186:187], v177 offset:0xfe00
	s_waitcnt lgkmcnt(8)
	v_mfma_f32_32x32x16_bf16 v[80:95], v[144:147], v[128:131], v[80:95]
	v_mfma_f32_32x32x16_bf16 v[80:95], v[148:151], v[132:135], v[80:95]
	v_mfma_f32_32x32x16_bf16 v[80:95], v[152:155], v[136:139], v[80:95]
	v_mfma_f32_32x32x16_bf16 v[80:95], v[156:159], v[140:143], v[80:95]
	s_waitcnt lgkmcnt(0)
	v_mfma_f32_32x32x16_bf16 v[96:111], v[166:169], v[128:131], v[96:111]
	v_mfma_f32_32x32x16_bf16 v[96:111], v[170:173], v[132:135], v[96:111]
	v_mfma_f32_32x32x16_bf16 v[96:111], v[180:183], v[136:139], v[96:111]
	v_mfma_f32_32x32x16_bf16 v[96:111], v[184:187], v[140:143], v[96:111]
	v_readlane_b32 s6, v255, 31
	v_readlane_b32 s7, v255, 32
	v_readlane_b32 s12, v255, 49
	v_readlane_b32 s13, v255, 50
	v_mov_b64_e32 v[128:129], s[6:7]
	v_readlane_b32 s6, v255, 35
	v_readlane_b32 s7, v255, 36
	flat_load_dword v130, v[128:129] sc0 sc1
	s_waitcnt vmcnt(0)
	s_ashr_i32 s13, s12, 31
	v_mov_b64_e32 v[128:129], s[6:7]
	flat_load_dword v131, v[128:129] sc0 sc1
	s_waitcnt vmcnt(0)
	s_lshl_b64 s[6:7], s[12:13], 11
	v_lshl_or_b32 v128, v175, 11, v174
	v_mov_b32_e32 v129, v161
	s_waitcnt lgkmcnt(0)
	s_barrier
	v_add_f32_e32 v158, v179, v204
	s_waitcnt lgkmcnt(0)
	v_readfirstlane_b32 s9, v130
	s_add_u32 s6, s9, s6
	v_readfirstlane_b32 s8, v131
	s_addc_u32 s7, s8, s7
	v_lshl_add_u64 v[156:157], s[6:7], 0, v[128:129]
	flat_load_dwordx4 v[128:131], v[156:157]
	flat_load_dwordx4 v[132:135], v[156:157] offset:32
	flat_load_dwordx4 v[136:139], v[156:157] offset:64
	flat_load_dwordx4 v[140:143], v[156:157] offset:96
	flat_load_dwordx4 v[144:147], v[156:157] offset:128
	flat_load_dwordx4 v[148:151], v[156:157] offset:160
	flat_load_dwordx4 v[152:155], v[156:157] offset:192
	flat_load_dwordx4 v[166:169], v[156:157] offset:224
	v_readlane_b32 s6, v255, 51
	v_readlane_b32 s7, v255, 52
	s_add_u32 s4, s4, s6
	s_addc_u32 s5, s5, s7
	v_lshl_add_u64 v[156:157], s[4:5], 0, v[160:161]
	flat_load_dword v156, v[156:157]
	v_mov_b32_e32 v157, v158
	s_nop 1
	v_permlane32_swap_b32_e32 v158, v157
	v_add_f32_e32 v157, v158, v157
	s_mul_i32 s5, s12, 0x6800
	s_mul_hi_i32 s4, s12, 0x6800
	s_add_u32 s2, s2, s5
	s_addc_u32 s3, s3, s4
	s_add_u32 s4, s2, 0x1000
	s_addc_u32 s5, s3, 0
	v_readlane_b32 s2, v255, 27
	s_waitcnt vmcnt(0) lgkmcnt(0)
	v_max_f32_e32 v156, v156, v156
	v_max_f32_e64 v156, |v157|, v156
	v_rcp_f32_e32 v194, v156
	s_nop 0
	v_mul_f32_e32 v196, v113, v194
	v_mul_f32_e32 v213, v115, v194
	v_mul_f32_e32 v195, v112, v194
	v_mul_f32_e32 v197, v114, v194
	v_mul_f32_e32 v217, v119, v194
	v_mul_f32_e32 v119, v52, v194
	v_mul_f32_e32 v115, v54, v194
	v_mul_f32_e32 v54, v56, v194
	v_mul_f32_e32 v52, v57, v194
	v_mul_f32_e32 v56, v196, v196
	v_mul_f32_e32 v57, v213, v213
	v_mul_f32_e32 v215, v117, v194
	v_fmac_f32_e32 v56, v195, v195
	v_fmac_f32_e32 v57, v197, v197
	v_mul_f32_e32 v214, v116, v194
	v_mul_f32_e32 v216, v118, v194
	v_mul_f32_e32 v114, v50, v194
	v_mul_f32_e32 v50, v58, v194
	v_add_f32_e32 v56, v56, v57
	v_mul_f32_e32 v57, v215, v215
	v_mul_f32_e32 v58, v217, v217
	v_mul_f32_e32 v219, v121, v194
	v_mul_f32_e32 v210, v123, v194
	v_fmac_f32_e32 v57, v214, v214
	v_fmac_f32_e32 v58, v216, v216
	v_mul_f32_e32 v218, v120, v194
	v_mul_f32_e32 v212, v122, v194
	v_mul_f32_e32 v118, v48, v194
	v_mul_f32_e32 v48, v59, v194
	v_add_f32_e32 v57, v57, v58
	v_mul_f32_e32 v58, v219, v219
	v_mul_f32_e32 v59, v210, v210
	v_mul_f32_e32 v221, v125, v194
	v_mul_f32_e32 v211, v127, v194
	v_fmac_f32_e32 v58, v218, v218
	v_fmac_f32_e32 v59, v212, v212
	v_mul_f32_e32 v220, v124, v194
	v_mul_f32_e32 v222, v126, v194
	v_mul_f32_e32 v113, v55, v194
	v_mul_f32_e32 v55, v60, v194
	v_add_f32_e32 v58, v58, v59
	v_mul_f32_e32 v59, v221, v221
	v_mul_f32_e32 v60, v211, v211
	v_fmac_f32_e32 v59, v220, v220
	v_fmac_f32_e32 v60, v222, v222
	v_add_f32_e32 v59, v59, v60
	v_mul_f32_e32 v206, v1, v194
	v_mul_f32_e32 v202, v3, v194
	v_add_f32_e32 v56, v56, v57
	v_add_f32_e32 v57, v58, v59
	v_mul_f32_e32 v208, v0, v194
	v_mul_f32_e32 v204, v2, v194
	v_add_f32_e32 v56, v56, v57
	v_mul_f32_e32 v57, v206, v206
	v_mul_f32_e32 v58, v202, v202
	v_mul_f32_e32 v207, v5, v194
	v_mul_f32_e32 v203, v7, v194
	v_fmac_f32_e32 v57, v208, v208
	v_fmac_f32_e32 v58, v204, v204
	v_mul_f32_e32 v209, v4, v194
	v_mul_f32_e32 v205, v6, v194
	v_add_f32_e32 v57, v57, v58
	v_mul_f32_e32 v58, v207, v207
	v_mul_f32_e32 v59, v203, v203
	v_mul_f32_e32 v198, v9, v194
	v_mul_f32_e32 v190, v11, v194
	v_fmac_f32_e32 v58, v209, v209
	v_fmac_f32_e32 v59, v205, v205
	v_mul_f32_e32 v200, v8, v194
	v_mul_f32_e32 v192, v10, v194
	v_add_f32_e32 v58, v58, v59
	v_mul_f32_e32 v59, v198, v198
	v_mul_f32_e32 v60, v190, v190
	v_mul_f32_e32 v199, v13, v194
	v_mul_f32_e32 v191, v15, v194
	v_fmac_f32_e32 v59, v200, v200
	v_fmac_f32_e32 v60, v192, v192
	v_mul_f32_e32 v201, v12, v194
	v_mul_f32_e32 v193, v14, v194
	v_mul_f32_e32 v117, v53, v194
	v_mul_f32_e32 v53, v61, v194
	v_add_f32_e32 v59, v59, v60
	v_mul_f32_e32 v60, v199, v199
	v_mul_f32_e32 v61, v191, v191
	v_fmac_f32_e32 v60, v201, v201
	v_fmac_f32_e32 v61, v193, v193
	v_add_f32_e32 v60, v60, v61
	v_add_f32_e32 v57, v57, v58
	v_add_f32_e32 v58, v59, v60
	v_mul_f32_e32 v186, v17, v194
	v_mul_f32_e32 v182, v19, v194
	v_add_f32_e32 v57, v57, v58
	v_mul_f32_e32 v188, v16, v194
	v_mul_f32_e32 v184, v18, v194
	v_add_f32_e32 v56, v56, v57
	v_mul_f32_e32 v57, v186, v186
	v_mul_f32_e32 v58, v182, v182
	v_mul_f32_e32 v187, v21, v194
	v_mul_f32_e32 v183, v23, v194
	v_fmac_f32_e32 v57, v188, v188
	v_fmac_f32_e32 v58, v184, v184
	v_mul_f32_e32 v189, v20, v194
	v_mul_f32_e32 v185, v22, v194
	v_add_f32_e32 v57, v57, v58
	v_mul_f32_e32 v58, v187, v187
	v_mul_f32_e32 v59, v183, v183
	v_mul_f32_e32 v178, v25, v194
	v_mul_f32_e32 v171, v27, v194
	v_fmac_f32_e32 v58, v189, v189
	v_fmac_f32_e32 v59, v185, v185
	v_mul_f32_e32 v180, v24, v194
	v_mul_f32_e32 v173, v26, v194
	v_add_f32_e32 v58, v58, v59
	v_mul_f32_e32 v59, v178, v178
	v_mul_f32_e32 v60, v171, v171
	v_mul_f32_e32 v179, v29, v194
	v_mul_f32_e32 v172, v31, v194
	v_fmac_f32_e32 v59, v180, v180
	v_fmac_f32_e32 v60, v173, v173
	v_mul_f32_e32 v181, v28, v194
	v_mul_f32_e32 v177, v30, v194
	v_add_f32_e32 v59, v59, v60
	v_mul_f32_e32 v60, v179, v179
	v_mul_f32_e32 v61, v172, v172
	v_fmac_f32_e32 v60, v181, v181
	v_fmac_f32_e32 v61, v177, v177
	v_add_f32_e32 v60, v60, v61
	v_add_f32_e32 v57, v57, v58
	v_add_f32_e32 v58, v59, v60
	v_mul_f32_e32 v160, v33, v194
	v_mul_f32_e32 v156, v35, v194
	v_add_f32_e32 v57, v57, v58
	v_mul_f32_e32 v163, v32, v194
	v_mul_f32_e32 v158, v34, v194
	v_add_f32_e32 v56, v57, v56
	v_mul_f32_e32 v57, v160, v160
	v_mul_f32_e32 v58, v156, v156
	v_mul_f32_e32 v162, v37, v194
	v_mul_f32_e32 v157, v39, v194
	v_fmac_f32_e32 v57, v163, v163
	v_fmac_f32_e32 v58, v158, v158
	v_mul_f32_e32 v170, v36, v194
	v_mul_f32_e32 v159, v38, v194
	v_add_f32_e32 v57, v57, v58
	v_mul_f32_e32 v58, v162, v162
	v_mul_f32_e32 v59, v157, v157
	v_mul_f32_e32 v124, v41, v194
	v_mul_f32_e32 v120, v43, v194
	v_fmac_f32_e32 v58, v170, v170
	v_fmac_f32_e32 v59, v159, v159
	v_mul_f32_e32 v126, v40, v194
	v_mul_f32_e32 v122, v42, v194
	v_add_f32_e32 v58, v58, v59
	v_mul_f32_e32 v59, v124, v124
	v_mul_f32_e32 v60, v120, v120
	v_mul_f32_e32 v125, v45, v194
	v_mul_f32_e32 v121, v47, v194
	v_fmac_f32_e32 v59, v126, v126
	v_fmac_f32_e32 v60, v122, v122
	v_mul_f32_e32 v127, v44, v194
	v_mul_f32_e32 v123, v46, v194
	v_add_f32_e32 v59, v59, v60
	v_mul_f32_e32 v60, v125, v125
	v_mul_f32_e32 v61, v121, v121
	v_fmac_f32_e32 v60, v127, v127
	v_fmac_f32_e32 v61, v123, v123
	v_add_f32_e32 v60, v60, v61
	v_add_f32_e32 v57, v57, v58
	v_add_f32_e32 v58, v59, v60
	v_mul_f32_e32 v116, v49, v194
	v_mul_f32_e32 v112, v51, v194
	v_add_f32_e32 v57, v57, v58
	v_add_f32_e32 v56, v57, v56
	v_mul_f32_e32 v57, v116, v116
	v_mul_f32_e32 v58, v112, v112
	v_fmac_f32_e32 v57, v118, v118
	v_fmac_f32_e32 v58, v114, v114
	v_add_f32_e32 v57, v57, v58
	v_mul_f32_e32 v58, v117, v117
	v_mul_f32_e32 v59, v113, v113
	v_fmac_f32_e32 v58, v119, v119
	v_fmac_f32_e32 v59, v115, v115
	v_add_f32_e32 v58, v58, v59
	v_mul_f32_e32 v59, v52, v52
	v_mul_f32_e32 v60, v48, v48
	v_mul_f32_e32 v49, v63, v194
	v_fmac_f32_e32 v59, v54, v54
	v_fmac_f32_e32 v60, v50, v50
	v_mul_f32_e32 v51, v62, v194
	v_add_f32_e32 v59, v59, v60
	v_mul_f32_e32 v60, v53, v53
	v_mul_f32_e32 v61, v49, v49
	v_fmac_f32_e32 v60, v55, v55
	v_fmac_f32_e32 v61, v51, v51
	v_add_f32_e32 v60, v60, v61
	v_add_f32_e32 v57, v57, v58
	v_add_f32_e32 v58, v59, v60
	v_mul_f32_e32 v44, v65, v194
	v_mul_f32_e32 v40, v67, v194
	v_add_f32_e32 v57, v57, v58
	v_mul_f32_e32 v46, v64, v194
	v_mul_f32_e32 v42, v66, v194
	v_add_f32_e32 v56, v57, v56
	v_mul_f32_e32 v57, v44, v44
	v_mul_f32_e32 v58, v40, v40
	v_mul_f32_e32 v45, v69, v194
	v_mul_f32_e32 v41, v71, v194
	v_fmac_f32_e32 v57, v46, v46
	v_fmac_f32_e32 v58, v42, v42
	v_mul_f32_e32 v47, v68, v194
	v_mul_f32_e32 v43, v70, v194
	v_add_f32_e32 v57, v57, v58
	v_mul_f32_e32 v58, v45, v45
	v_mul_f32_e32 v59, v41, v41
	v_mul_f32_e32 v36, v73, v194
	v_mul_f32_e32 v32, v75, v194
	v_fmac_f32_e32 v58, v47, v47
	v_fmac_f32_e32 v59, v43, v43
	v_mul_f32_e32 v38, v72, v194
	v_mul_f32_e32 v34, v74, v194
	v_add_f32_e32 v58, v58, v59
	v_mul_f32_e32 v59, v36, v36
	v_mul_f32_e32 v60, v32, v32
	v_mul_f32_e32 v37, v77, v194
	v_mul_f32_e32 v33, v79, v194
	v_fmac_f32_e32 v59, v38, v38
	v_fmac_f32_e32 v60, v34, v34
	v_mul_f32_e32 v39, v76, v194
	v_mul_f32_e32 v35, v78, v194
	v_add_f32_e32 v59, v59, v60
	v_mul_f32_e32 v60, v37, v37
	v_mul_f32_e32 v61, v33, v33
	v_fmac_f32_e32 v60, v39, v39
	v_fmac_f32_e32 v61, v35, v35
	v_mul_f32_e32 v31, v84, v194
	v_add_f32_e32 v60, v60, v61
	v_mul_u32_u24_e32 v84, 0x6800, v175
	v_add_f32_e32 v57, v57, v58
	v_add_f32_e32 v58, v59, v60
	v_lshl_or_b32 v59, v176, 3, v84
	global_load_dwordx2 v[68:69], v59, s[4:5]
	global_load_dwordx2 v[70:71], v59, s[4:5] offset:16
	global_load_dwordx2 v[72:73], v59, s[4:5] offset:32
	global_load_dwordx2 v[74:75], v59, s[4:5] offset:48
	v_mul_f32_e32 v30, v80, v194
	v_mul_f32_e32 v28, v81, v194
	v_mul_f32_e32 v26, v82, v194
	v_mul_f32_e32 v24, v83, v194
	v_add_f32_e32 v57, v57, v58
	global_load_dwordx2 v[76:77], v59, s[4:5] offset:64
	global_load_dwordx2 v[78:79], v59, s[4:5] offset:80
	global_load_dwordx2 v[80:81], v59, s[4:5] offset:96
	global_load_dwordx2 v[82:83], v59, s[4:5] offset:112
	v_add_f32_e32 v56, v57, v56
	v_mul_f32_e32 v57, v28, v28
	v_mul_f32_e32 v58, v24, v24
	v_mul_f32_e32 v29, v85, v194
	v_mul_f32_e32 v25, v87, v194
	v_fmac_f32_e32 v57, v30, v30
	v_fmac_f32_e32 v58, v26, v26
	v_mul_f32_e32 v27, v86, v194
	v_add_f32_e32 v57, v57, v58
	v_mul_f32_e32 v58, v29, v29
	v_mul_f32_e32 v60, v25, v25
	v_mul_f32_e32 v20, v89, v194
	v_mul_f32_e32 v16, v91, v194
	v_fmac_f32_e32 v58, v31, v31
	v_fmac_f32_e32 v60, v27, v27
	v_mul_f32_e32 v22, v88, v194
	v_mul_f32_e32 v18, v90, v194
	v_add_f32_e32 v58, v58, v60
	v_mul_f32_e32 v60, v20, v20
	v_mul_f32_e32 v61, v16, v16
	v_mul_f32_e32 v21, v93, v194
	v_mul_f32_e32 v17, v95, v194
	v_fmac_f32_e32 v60, v22, v22
	v_fmac_f32_e32 v61, v18, v18
	v_mul_f32_e32 v23, v92, v194
	v_mul_f32_e32 v19, v94, v194
	v_add_f32_e32 v60, v60, v61
	v_mul_f32_e32 v61, v21, v21
	v_mul_f32_e32 v62, v17, v17
	v_fmac_f32_e32 v61, v23, v23
	v_fmac_f32_e32 v62, v19, v19
	v_add_f32_e32 v61, v61, v62
	v_add_f32_e32 v57, v57, v58
	v_add_f32_e32 v58, v60, v61
	v_mul_f32_e32 v12, v97, v194
	v_mul_f32_e32 v8, v99, v194
	v_add_f32_e32 v57, v57, v58
	v_mul_f32_e32 v14, v96, v194
	v_mul_f32_e32 v10, v98, v194
	v_add_f32_e32 v56, v57, v56
	v_mul_f32_e32 v57, v12, v12
	v_mul_f32_e32 v58, v8, v8
	v_mul_f32_e32 v13, v101, v194
	v_mul_f32_e32 v9, v103, v194
	v_fmac_f32_e32 v57, v14, v14
	v_fmac_f32_e32 v58, v10, v10
	v_mul_f32_e32 v15, v100, v194
	v_mul_f32_e32 v11, v102, v194
	v_add_f32_e32 v57, v57, v58
	v_mul_f32_e32 v58, v13, v13
	v_mul_f32_e32 v60, v9, v9
	v_mul_f32_e32 v4, v105, v194
	v_mul_f32_e32 v0, v107, v194
	v_fmac_f32_e32 v58, v15, v15
	v_fmac_f32_e32 v60, v11, v11
	v_mul_f32_e32 v6, v104, v194
	v_mul_f32_e32 v2, v106, v194
	v_add_f32_e32 v58, v58, v60
	v_mul_f32_e32 v60, v4, v4
	v_mul_f32_e32 v61, v0, v0
	v_mul_f32_e32 v5, v109, v194
	v_mul_f32_e32 v1, v111, v194
	v_fmac_f32_e32 v60, v6, v6
	v_fmac_f32_e32 v61, v2, v2
	v_mul_f32_e32 v7, v108, v194
	v_mul_f32_e32 v3, v110, v194
	v_add_f32_e32 v60, v60, v61
	v_mul_f32_e32 v61, v5, v5
	v_mul_f32_e32 v62, v1, v1
	v_fmac_f32_e32 v61, v7, v7
	v_fmac_f32_e32 v62, v3, v3
	v_add_f32_e32 v61, v61, v62
	v_add_f32_e32 v57, v57, v58
	v_add_f32_e32 v58, v60, v61
	v_add_f32_e32 v57, v57, v58
	v_add_f32_e32 v56, v57, v56
	v_mov_b32_e32 v57, v56
	s_nop 1
	v_permlane32_swap_b32_e32 v56, v57
	v_add_f32_e32 v56, v56, v57
	v_fmamk_f32 v56, v56, 0x3b800000, v254
	v_rsq_f32_e32 v56, v56
	v_add_u32_e32 v57, s2, v174
	ds_read_b128 v[60:63], v57
	ds_read_b128 v[64:67], v57 offset:32
	v_mul_f32_e32 v58, v195, v56
	v_mul_f32_e32 v54, v54, v56
	v_mul_f32_e32 v52, v52, v56
	s_waitcnt lgkmcnt(1)
	v_mul_f32_e32 v58, v58, v60
	v_mul_f32_e32 v60, v214, v56
	s_waitcnt lgkmcnt(0)
	v_mul_f32_e32 v60, v60, v64
	v_mul_f32_e32 v64, v196, v56
	v_mul_f32_e32 v61, v64, v61
	v_mul_f32_e32 v64, v215, v56
	v_mul_f32_e32 v64, v64, v65
	v_mul_f32_e32 v65, v197, v56
	v_mul_f32_e32 v62, v65, v62
	v_mul_f32_e32 v65, v216, v56
	v_mul_f32_e32 v65, v65, v66
	v_mul_f32_e32 v66, v213, v56
	v_mul_f32_e32 v63, v66, v63
	v_mul_f32_e32 v66, v217, v56
	v_mul_f32_e32 v66, v66, v67
	s_waitcnt vmcnt(7)
	v_lshlrev_b32_e32 v67, 16, v68
	v_mul_f32_e32 v58, v58, v67
	v_and_b32_e32 v67, 0xffff0000, v68
	v_mul_f32_e32 v61, v61, v67
	v_lshlrev_b32_e32 v67, 16, v69
	v_mul_f32_e32 v62, v62, v67
	v_and_b32_e32 v67, 0xffff0000, v69
	v_mul_f32_e32 v63, v63, v67
	s_waitcnt vmcnt(6)
	v_lshlrev_b32_e32 v67, 16, v70
	v_mul_f32_e32 v67, v60, v67
	v_and_b32_e32 v60, 0xffff0000, v70
	v_mul_f32_e32 v64, v64, v60
	v_lshlrev_b32_e32 v60, 16, v71
	v_mul_f32_e32 v65, v65, v60
	v_and_b32_e32 v60, 0xffff0000, v71
	v_mul_f32_e32 v66, v66, v60
	v_cvt_pk_bf16_f32 v60, v58, v61
	v_cvt_pk_bf16_f32 v61, v62, v63
	v_cvt_pk_bf16_f32 v62, v67, v64
	v_cvt_pk_bf16_f32 v63, v65, v66
	ds_read_b128 v[64:67], v57 offset:64
	ds_read_b128 v[68:71], v57 offset:96
	v_permlane32_swap_b32_e32 v60, v62
	v_permlane32_swap_b32_e32 v61, v63
	v_or_b32_e32 v58, v174, v84
	global_store_dwordx4 v58, v[60:63], s[4:5]
	v_mul_f32_e32 v50, v50, v56
	v_mul_f32_e32 v48, v48, v56
	v_mul_f32_e32 v60, v218, v56
	v_mul_f32_e32 v61, v220, v56
	s_waitcnt lgkmcnt(1)
	v_mul_f32_e32 v60, v60, v64
	s_waitcnt lgkmcnt(0)
	v_mul_f32_e32 v61, v61, v68
	v_mul_f32_e32 v62, v219, v56
	s_waitcnt vmcnt(6)
	v_lshlrev_b32_e32 v68, 16, v72
	v_mul_f32_e32 v62, v62, v65
	v_mul_f32_e32 v64, v212, v56
	v_mul_f32_e32 v60, v60, v68
	v_and_b32_e32 v68, 0xffff0000, v72
	v_mul_f32_e32 v64, v64, v66
	v_mul_f32_e32 v66, v210, v56
	v_mul_f32_e32 v62, v62, v68
	v_lshlrev_b32_e32 v68, 16, v73
	v_mul_f32_e32 v66, v66, v67
	v_mul_f32_e32 v64, v64, v68
	v_and_b32_e32 v68, 0xffff0000, v73
	v_mul_f32_e32 v63, v221, v56
	v_mul_f32_e32 v66, v66, v68
	s_waitcnt vmcnt(5)
	v_lshlrev_b32_e32 v68, 16, v74
	v_mul_f32_e32 v63, v63, v69
	v_mul_f32_e32 v65, v222, v56
	v_mul_f32_e32 v68, v61, v68
	v_and_b32_e32 v61, 0xffff0000, v74
	v_mul_f32_e32 v65, v65, v70
	v_mul_f32_e32 v67, v211, v56
	v_mul_f32_e32 v63, v63, v61
	v_lshlrev_b32_e32 v61, 16, v75
	v_mul_f32_e32 v67, v67, v71
	v_mul_f32_e32 v65, v65, v61
	v_and_b32_e32 v61, 0xffff0000, v75
	v_mul_f32_e32 v67, v67, v61
	v_cvt_pk_bf16_f32 v60, v60, v62
	v_cvt_pk_bf16_f32 v61, v64, v66
	v_cvt_pk_bf16_f32 v62, v68, v63
	v_cvt_pk_bf16_f32 v63, v65, v67
	v_mul_f32_e32 v68, v208, v56
	v_permlane32_swap_b32_e32 v60, v62
	v_permlane32_swap_b32_e32 v61, v63
	global_store_dwordx4 v58, v[60:63], s[4:5] offset:32
	global_load_dwordx2 v[72:73], v59, s[4:5] offset:128
	global_load_dwordx2 v[74:75], v59, s[4:5] offset:144
	global_load_dwordx2 v[84:85], v59, s[4:5] offset:160
	global_load_dwordx2 v[86:87], v59, s[4:5] offset:176
	ds_read_b128 v[60:63], v57 offset:128
	ds_read_b128 v[64:67], v57 offset:160
	v_mul_f32_e32 v55, v55, v56
	v_mul_f32_e32 v53, v53, v56
	v_mul_f32_e32 v51, v51, v56
	s_waitcnt lgkmcnt(1)
	v_mul_f32_e32 v60, v68, v60
	v_mul_f32_e32 v68, v209, v56
	s_waitcnt lgkmcnt(0)
	v_mul_f32_e32 v64, v68, v64
	v_mul_f32_e32 v68, v206, v56
	v_mul_f32_e32 v61, v68, v61
	v_mul_f32_e32 v68, v207, v56
	v_mul_f32_e32 v65, v68, v65
	v_mul_f32_e32 v68, v204, v56
	v_mul_f32_e32 v62, v68, v62
	v_mul_f32_e32 v68, v205, v56
	v_mul_f32_e32 v66, v68, v66
	v_mul_f32_e32 v68, v202, v56
	v_mul_f32_e32 v63, v68, v63
	v_mul_f32_e32 v68, v203, v56
	v_mul_f32_e32 v67, v68, v67
	s_waitcnt vmcnt(9)
	v_lshlrev_b32_e32 v68, 16, v76
	v_mul_f32_e32 v60, v60, v68
	v_and_b32_e32 v68, 0xffff0000, v76
	v_mul_f32_e32 v61, v61, v68
	v_lshlrev_b32_e32 v68, 16, v77
	v_mul_f32_e32 v62, v62, v68
	v_and_b32_e32 v68, 0xffff0000, v77
	v_mul_f32_e32 v63, v63, v68
	s_waitcnt vmcnt(8)
	v_lshlrev_b32_e32 v68, 16, v78
	v_mul_f32_e32 v64, v64, v68
	v_and_b32_e32 v68, 0xffff0000, v78
	v_mul_f32_e32 v65, v65, v68
	v_lshlrev_b32_e32 v68, 16, v79
	v_mul_f32_e32 v66, v66, v68
	v_and_b32_e32 v68, 0xffff0000, v79
	v_mul_f32_e32 v67, v67, v68
	v_cvt_pk_bf16_f32 v60, v60, v61
	v_cvt_pk_bf16_f32 v61, v62, v63
	v_cvt_pk_bf16_f32 v62, v64, v65
	v_cvt_pk_bf16_f32 v63, v66, v67
	ds_read_b128 v[64:67], v57 offset:192
	ds_read_b128 v[68:71], v57 offset:224
	v_permlane32_swap_b32_e32 v60, v62
	v_permlane32_swap_b32_e32 v61, v63
	global_store_dwordx4 v58, v[60:63], s[4:5] offset:64
	v_mul_f32_e32 v49, v49, v56
	v_mul_f32_e32 v46, v46, v56
	v_mul_f32_e32 v60, v200, v56
	v_mul_f32_e32 v61, v201, v56
	s_waitcnt lgkmcnt(1)
	v_mul_f32_e32 v60, v60, v64
	s_waitcnt lgkmcnt(0)
	v_mul_f32_e32 v61, v61, v68
	v_mul_f32_e32 v62, v198, v56
	s_waitcnt vmcnt(8)
	v_lshlrev_b32_e32 v68, 16, v80
	v_mul_f32_e32 v62, v62, v65
	v_mul_f32_e32 v64, v192, v56
	v_mul_f32_e32 v60, v60, v68
	v_and_b32_e32 v68, 0xffff0000, v80
	v_mul_f32_e32 v64, v64, v66
	v_mul_f32_e32 v66, v190, v56
	v_mul_f32_e32 v62, v62, v68
	v_lshlrev_b32_e32 v68, 16, v81
	v_mul_f32_e32 v66, v66, v67
	v_mul_f32_e32 v64, v64, v68
	v_and_b32_e32 v68, 0xffff0000, v81
	v_mul_f32_e32 v63, v199, v56
	v_mul_f32_e32 v66, v66, v68
	s_waitcnt vmcnt(7)
	v_lshlrev_b32_e32 v68, 16, v82
	v_mul_f32_e32 v63, v63, v69
	v_mul_f32_e32 v65, v193, v56
	v_mul_f32_e32 v68, v61, v68
	v_and_b32_e32 v61, 0xffff0000, v82
	v_mul_f32_e32 v65, v65, v70
	v_mul_f32_e32 v67, v191, v56
	v_mul_f32_e32 v63, v63, v61
	v_lshlrev_b32_e32 v61, 16, v83
	v_mul_f32_e32 v67, v67, v71
	v_mul_f32_e32 v65, v65, v61
	v_and_b32_e32 v61, 0xffff0000, v83
	v_mul_f32_e32 v67, v67, v61
	v_cvt_pk_bf16_f32 v60, v60, v62
	v_cvt_pk_bf16_f32 v61, v64, v66
	v_cvt_pk_bf16_f32 v62, v68, v63
	v_cvt_pk_bf16_f32 v63, v65, v67
	v_or_b32_e32 v64, 64, v58
	v_permlane32_swap_b32_e32 v60, v62
	v_permlane32_swap_b32_e32 v61, v63
	global_store_dwordx4 v64, v[60:63], s[4:5] offset:32
	global_load_dwordx2 v[76:77], v59, s[4:5] offset:192
	global_load_dwordx2 v[78:79], v59, s[4:5] offset:208
	global_load_dwordx2 v[80:81], v59, s[4:5] offset:224
	global_load_dwordx2 v[82:83], v59, s[4:5] offset:240
	ds_read_b128 v[60:63], v57 offset:256
	ds_read_b128 v[64:67], v57 offset:288
	v_mul_f32_e32 v68, v188, v56
	v_mul_f32_e32 v44, v44, v56
	v_mul_f32_e32 v42, v42, v56
	s_waitcnt lgkmcnt(1)
	v_mul_f32_e32 v60, v68, v60
	v_mul_f32_e32 v68, v189, v56
	s_waitcnt lgkmcnt(0)
	v_mul_f32_e32 v64, v68, v64
	v_mul_f32_e32 v68, v186, v56
	v_mul_f32_e32 v61, v68, v61
	v_mul_f32_e32 v68, v187, v56
	v_mul_f32_e32 v65, v68, v65
	v_mul_f32_e32 v68, v184, v56
	v_mul_f32_e32 v62, v68, v62
	v_mul_f32_e32 v68, v185, v56
	v_mul_f32_e32 v66, v68, v66
	v_mul_f32_e32 v68, v182, v56
	v_mul_f32_e32 v63, v68, v63
	v_mul_f32_e32 v68, v183, v56
	v_mul_f32_e32 v67, v68, v67
	s_waitcnt vmcnt(9)
	v_lshlrev_b32_e32 v68, 16, v72
	v_mul_f32_e32 v60, v60, v68
	v_and_b32_e32 v68, 0xffff0000, v72
	v_mul_f32_e32 v61, v61, v68
	v_lshlrev_b32_e32 v68, 16, v73
	v_mul_f32_e32 v62, v62, v68
	v_and_b32_e32 v68, 0xffff0000, v73
	v_mul_f32_e32 v63, v63, v68
	s_waitcnt vmcnt(8)
	v_lshlrev_b32_e32 v68, 16, v74
	v_mul_f32_e32 v64, v64, v68
	v_and_b32_e32 v68, 0xffff0000, v74
	v_mul_f32_e32 v65, v65, v68
	v_lshlrev_b32_e32 v68, 16, v75
	v_mul_f32_e32 v66, v66, v68
	v_and_b32_e32 v68, 0xffff0000, v75
	v_mul_f32_e32 v67, v67, v68
	v_cvt_pk_bf16_f32 v60, v60, v61
	v_cvt_pk_bf16_f32 v61, v62, v63
	v_cvt_pk_bf16_f32 v62, v64, v65
	v_cvt_pk_bf16_f32 v63, v66, v67
	ds_read_b128 v[64:67], v57 offset:320
	ds_read_b128 v[68:71], v57 offset:352
	v_permlane32_swap_b32_e32 v60, v62
	v_permlane32_swap_b32_e32 v61, v63
	global_store_dwordx4 v58, v[60:63], s[4:5] offset:128
	v_mul_f32_e32 v40, v40, v56
	v_mul_f32_e32 v47, v47, v56
	v_mul_f32_e32 v60, v180, v56
	v_mul_f32_e32 v61, v181, v56
	s_waitcnt lgkmcnt(1)
	v_mul_f32_e32 v60, v60, v64
	s_waitcnt lgkmcnt(0)
	v_mul_f32_e32 v61, v61, v68
	v_mul_f32_e32 v62, v178, v56
	s_waitcnt vmcnt(8)
	v_lshlrev_b32_e32 v68, 16, v84
	v_mul_f32_e32 v62, v62, v65
	v_mul_f32_e32 v64, v173, v56
	v_mul_f32_e32 v60, v60, v68
	v_and_b32_e32 v68, 0xffff0000, v84
	v_mul_f32_e32 v64, v64, v66
	v_mul_f32_e32 v66, v171, v56
	v_mul_f32_e32 v62, v62, v68
	v_lshlrev_b32_e32 v68, 16, v85
	v_mul_f32_e32 v66, v66, v67
	v_mul_f32_e32 v64, v64, v68
	v_and_b32_e32 v68, 0xffff0000, v85
	v_mul_f32_e32 v63, v179, v56
	v_mul_f32_e32 v66, v66, v68
	s_waitcnt vmcnt(7)
	v_lshlrev_b32_e32 v68, 16, v86
	v_mul_f32_e32 v63, v63, v69
	v_mul_f32_e32 v65, v177, v56
	v_mul_f32_e32 v68, v61, v68
	v_and_b32_e32 v61, 0xffff0000, v86
	v_mul_f32_e32 v65, v65, v70
	v_mul_f32_e32 v67, v172, v56
	v_mul_f32_e32 v63, v63, v61
	v_lshlrev_b32_e32 v61, 16, v87
	v_mul_f32_e32 v67, v67, v71
	v_mul_f32_e32 v65, v65, v61
	v_and_b32_e32 v61, 0xffff0000, v87
	v_mul_f32_e32 v67, v67, v61
	v_cvt_pk_bf16_f32 v60, v60, v62
	v_cvt_pk_bf16_f32 v61, v64, v66
	v_cvt_pk_bf16_f32 v62, v68, v63
	v_cvt_pk_bf16_f32 v63, v65, v67
	v_or_b32_e32 v64, 0x80, v58
	v_permlane32_swap_b32_e32 v60, v62
	v_permlane32_swap_b32_e32 v61, v63
	global_store_dwordx4 v64, v[60:63], s[4:5] offset:32
	global_load_dwordx2 v[72:73], v59, s[4:5] offset:256
	global_load_dwordx2 v[74:75], v59, s[4:5] offset:272
	global_load_dwordx2 v[84:85], v59, s[4:5] offset:288
	global_load_dwordx2 v[86:87], v59, s[4:5] offset:304
	ds_read_b128 v[60:63], v57 offset:384
	ds_read_b128 v[64:67], v57 offset:416
	v_mul_f32_e32 v68, v163, v56
	v_mul_f32_e32 v45, v45, v56
	v_mul_f32_e32 v43, v43, v56
	s_waitcnt lgkmcnt(1)
	v_mul_f32_e32 v60, v68, v60
	v_mul_f32_e32 v68, v170, v56
	s_waitcnt lgkmcnt(0)
	v_mul_f32_e32 v64, v68, v64
	v_mul_f32_e32 v68, v160, v56
	v_mul_f32_e32 v61, v68, v61
	v_mul_f32_e32 v68, v162, v56
	v_mul_f32_e32 v65, v68, v65
	v_mul_f32_e32 v68, v158, v56
	v_mul_f32_e32 v62, v68, v62
	v_mul_f32_e32 v68, v159, v56
	v_mul_f32_e32 v66, v68, v66
	v_mul_f32_e32 v68, v156, v56
	v_mul_f32_e32 v63, v68, v63
	v_mul_f32_e32 v68, v157, v56
	v_mul_f32_e32 v67, v68, v67
	s_waitcnt vmcnt(9)
	v_lshlrev_b32_e32 v68, 16, v76
	v_mul_f32_e32 v60, v60, v68
	v_and_b32_e32 v68, 0xffff0000, v76
	v_mul_f32_e32 v61, v61, v68
	v_lshlrev_b32_e32 v68, 16, v77
	v_mul_f32_e32 v62, v62, v68
	v_and_b32_e32 v68, 0xffff0000, v77
	v_mul_f32_e32 v63, v63, v68
	s_waitcnt vmcnt(8)
	v_lshlrev_b32_e32 v68, 16, v78
	v_mul_f32_e32 v64, v64, v68
	v_and_b32_e32 v68, 0xffff0000, v78
	v_mul_f32_e32 v65, v65, v68
	v_lshlrev_b32_e32 v68, 16, v79
	v_mul_f32_e32 v66, v66, v68
	v_and_b32_e32 v68, 0xffff0000, v79
	v_mul_f32_e32 v67, v67, v68
	v_cvt_pk_bf16_f32 v60, v60, v61
	v_cvt_pk_bf16_f32 v61, v62, v63
	v_cvt_pk_bf16_f32 v62, v64, v65
	v_cvt_pk_bf16_f32 v63, v66, v67
	ds_read_b128 v[64:67], v57 offset:448
	ds_read_b128 v[68:71], v57 offset:480
	v_permlane32_swap_b32_e32 v60, v62
	v_permlane32_swap_b32_e32 v61, v63
	global_store_dwordx4 v58, v[60:63], s[4:5] offset:192
	v_mul_f32_e32 v41, v41, v56
	v_mul_f32_e32 v38, v38, v56
	v_mul_f32_e32 v60, v126, v56
	v_mul_f32_e32 v61, v127, v56
	s_waitcnt lgkmcnt(1)
	v_mul_f32_e32 v60, v60, v64
	s_waitcnt lgkmcnt(0)
	v_mul_f32_e32 v61, v61, v68
	v_mul_f32_e32 v62, v124, v56
	s_waitcnt vmcnt(8)
	v_lshlrev_b32_e32 v68, 16, v80
	v_mul_f32_e32 v62, v62, v65
	v_mul_f32_e32 v64, v122, v56
	v_mul_f32_e32 v60, v60, v68
	v_and_b32_e32 v68, 0xffff0000, v80
	v_mul_f32_e32 v64, v64, v66
	v_mul_f32_e32 v66, v120, v56
	v_mul_f32_e32 v62, v62, v68
	v_lshlrev_b32_e32 v68, 16, v81
	v_mul_f32_e32 v66, v66, v67
	v_mul_f32_e32 v64, v64, v68
	v_and_b32_e32 v68, 0xffff0000, v81
	v_mul_f32_e32 v63, v125, v56
	v_mul_f32_e32 v66, v66, v68
	s_waitcnt vmcnt(7)
	v_lshlrev_b32_e32 v68, 16, v82
	v_mul_f32_e32 v63, v63, v69
	v_mul_f32_e32 v65, v123, v56
	v_mul_f32_e32 v68, v61, v68
	v_and_b32_e32 v61, 0xffff0000, v82
	v_mul_f32_e32 v65, v65, v70
	v_mul_f32_e32 v67, v121, v56
	v_mul_f32_e32 v63, v63, v61
	v_lshlrev_b32_e32 v61, 16, v83
	v_mul_f32_e32 v67, v67, v71
	v_mul_f32_e32 v65, v65, v61
	v_and_b32_e32 v61, 0xffff0000, v83
	v_mul_f32_e32 v67, v67, v61
	v_cvt_pk_bf16_f32 v60, v60, v62
	v_cvt_pk_bf16_f32 v61, v64, v66
	v_cvt_pk_bf16_f32 v62, v68, v63
	v_cvt_pk_bf16_f32 v63, v65, v67
	v_or_b32_e32 v64, 0xc0, v58
	v_permlane32_swap_b32_e32 v60, v62
	v_permlane32_swap_b32_e32 v61, v63
	global_store_dwordx4 v64, v[60:63], s[4:5] offset:32
	global_load_dwordx2 v[76:77], v59, s[4:5] offset:320
	global_load_dwordx2 v[78:79], v59, s[4:5] offset:336
	global_load_dwordx2 v[80:81], v59, s[4:5] offset:352
	global_load_dwordx2 v[82:83], v59, s[4:5] offset:368
	ds_read_b128 v[60:63], v57 offset:512
	ds_read_b128 v[64:67], v57 offset:544
	v_mul_f32_e32 v68, v118, v56
	v_mul_f32_e32 v36, v36, v56
	v_mul_f32_e32 v34, v34, v56
	s_waitcnt lgkmcnt(1)
	v_mul_f32_e32 v60, v68, v60
	v_mul_f32_e32 v68, v119, v56
	s_waitcnt lgkmcnt(0)
	v_mul_f32_e32 v64, v68, v64
	v_mul_f32_e32 v68, v116, v56
	v_mul_f32_e32 v61, v68, v61
	v_mul_f32_e32 v68, v117, v56
	v_mul_f32_e32 v65, v68, v65
	v_mul_f32_e32 v68, v114, v56
	v_mul_f32_e32 v62, v68, v62
	v_mul_f32_e32 v68, v115, v56
	v_mul_f32_e32 v66, v68, v66
	v_mul_f32_e32 v68, v112, v56
	v_mul_f32_e32 v63, v68, v63
	v_mul_f32_e32 v68, v113, v56
	v_mul_f32_e32 v67, v68, v67
	s_waitcnt vmcnt(9)
	v_lshlrev_b32_e32 v68, 16, v72
	v_mul_f32_e32 v60, v60, v68
	v_and_b32_e32 v68, 0xffff0000, v72
	v_mul_f32_e32 v61, v61, v68
	v_lshlrev_b32_e32 v68, 16, v73
	v_mul_f32_e32 v62, v62, v68
	v_and_b32_e32 v68, 0xffff0000, v73
	v_mul_f32_e32 v63, v63, v68
	s_waitcnt vmcnt(8)
	v_lshlrev_b32_e32 v68, 16, v74
	v_mul_f32_e32 v64, v64, v68
	v_and_b32_e32 v68, 0xffff0000, v74
	v_mul_f32_e32 v65, v65, v68
	v_lshlrev_b32_e32 v68, 16, v75
	v_mul_f32_e32 v66, v66, v68
	v_and_b32_e32 v68, 0xffff0000, v75
	v_mul_f32_e32 v67, v67, v68
	v_cvt_pk_bf16_f32 v60, v60, v61
	v_cvt_pk_bf16_f32 v61, v62, v63
	v_cvt_pk_bf16_f32 v62, v64, v65
	v_cvt_pk_bf16_f32 v63, v66, v67
	ds_read_b128 v[64:67], v57 offset:576
	ds_read_b128 v[68:71], v57 offset:608
	v_permlane32_swap_b32_e32 v60, v62
	v_permlane32_swap_b32_e32 v61, v63
	global_store_dwordx4 v58, v[60:63], s[4:5] offset:256
	s_waitcnt lgkmcnt(1)
	v_mul_f32_e32 v54, v54, v64
	v_mul_f32_e32 v52, v52, v65
	s_waitcnt vmcnt(8)
	v_lshlrev_b32_e32 v60, 16, v84
	v_mul_f32_e32 v54, v54, v60
	v_and_b32_e32 v60, 0xffff0000, v84
	v_mul_f32_e32 v50, v50, v66
	v_mul_f32_e32 v52, v52, v60
	v_lshlrev_b32_e32 v60, 16, v85
	v_mul_f32_e32 v48, v48, v67
	v_mul_f32_e32 v50, v50, v60
	v_and_b32_e32 v60, 0xffff0000, v85
	s_waitcnt lgkmcnt(0)
	v_mul_f32_e32 v55, v55, v68
	v_mul_f32_e32 v60, v48, v60
	s_waitcnt vmcnt(7)
	v_lshlrev_b32_e32 v48, 16, v86
	v_mul_f32_e32 v53, v53, v69
	v_mul_f32_e32 v55, v55, v48
	v_and_b32_e32 v48, 0xffff0000, v86
	v_mul_f32_e32 v51, v51, v70
	v_mul_f32_e32 v53, v53, v48
	v_lshlrev_b32_e32 v48, 16, v87
	v_mul_f32_e32 v49, v49, v71
	v_mul_f32_e32 v51, v51, v48
	v_and_b32_e32 v48, 0xffff0000, v87
	v_mul_f32_e32 v61, v49, v48
	v_cvt_pk_bf16_f32 v48, v54, v52
	v_cvt_pk_bf16_f32 v49, v50, v60
	v_cvt_pk_bf16_f32 v50, v55, v53
	v_cvt_pk_bf16_f32 v51, v51, v61
	v_or_b32_e32 v52, 0x100, v58
	v_permlane32_swap_b32_e32 v48, v50
	v_permlane32_swap_b32_e32 v49, v51
	global_store_dwordx4 v52, v[48:51], s[4:5] offset:32
	global_load_dwordx2 v[60:61], v59, s[4:5] offset:384
	global_load_dwordx2 v[62:63], v59, s[4:5] offset:400
	global_load_dwordx2 v[64:65], v59, s[4:5] offset:416
	global_load_dwordx2 v[66:67], v59, s[4:5] offset:432
	ds_read_b128 v[48:51], v57 offset:640
	ds_read_b128 v[52:55], v57 offset:672
	v_mul_f32_e32 v32, v32, v56
	v_mul_f32_e32 v39, v39, v56
	v_mul_f32_e32 v37, v37, v56
	s_waitcnt lgkmcnt(1)
	v_mul_f32_e32 v46, v46, v48
	s_waitcnt vmcnt(9)
	v_lshlrev_b32_e32 v48, 16, v76
	v_mul_f32_e32 v44, v44, v49
	v_mul_f32_e32 v46, v46, v48
	v_and_b32_e32 v48, 0xffff0000, v76
	v_mul_f32_e32 v42, v42, v50
	v_mul_f32_e32 v44, v44, v48
	v_lshlrev_b32_e32 v48, 16, v77
	v_mul_f32_e32 v40, v40, v51
	v_mul_f32_e32 v42, v42, v48
	v_and_b32_e32 v48, 0xffff0000, v77
	s_waitcnt lgkmcnt(0)
	v_mul_f32_e32 v47, v47, v52
	v_mul_f32_e32 v48, v40, v48
	s_waitcnt vmcnt(8)
	v_lshlrev_b32_e32 v40, 16, v78
	v_mul_f32_e32 v45, v45, v53
	v_mul_f32_e32 v47, v47, v40
	v_and_b32_e32 v40, 0xffff0000, v78
	v_mul_f32_e32 v43, v43, v54
	v_mul_f32_e32 v45, v45, v40
	v_lshlrev_b32_e32 v40, 16, v79
	v_mul_f32_e32 v41, v41, v55
	v_mul_f32_e32 v43, v43, v40
	v_and_b32_e32 v40, 0xffff0000, v79
	v_mul_f32_e32 v49, v41, v40
	v_cvt_pk_bf16_f32 v40, v46, v44
	v_cvt_pk_bf16_f32 v41, v42, v48
	v_cvt_pk_bf16_f32 v42, v47, v45
	v_cvt_pk_bf16_f32 v43, v43, v49
	ds_read_b128 v[44:47], v57 offset:704
	ds_read_b128 v[48:51], v57 offset:736
	v_permlane32_swap_b32_e32 v40, v42
	v_permlane32_swap_b32_e32 v41, v43
	global_store_dwordx4 v58, v[40:43], s[4:5] offset:320
	s_waitcnt lgkmcnt(1)
	v_mul_f32_e32 v38, v38, v44
	v_mul_f32_e32 v36, v36, v45
	s_waitcnt vmcnt(8)
	v_lshlrev_b32_e32 v40, 16, v80
	v_mul_f32_e32 v38, v38, v40
	v_and_b32_e32 v40, 0xffff0000, v80
	v_mul_f32_e32 v34, v34, v46
	v_mul_f32_e32 v36, v36, v40
	v_lshlrev_b32_e32 v40, 16, v81
	v_mul_f32_e32 v32, v32, v47
	v_mul_f32_e32 v34, v34, v40
	v_and_b32_e32 v40, 0xffff0000, v81
	s_waitcnt lgkmcnt(0)
	v_mul_f32_e32 v39, v39, v48
	v_mul_f32_e32 v40, v32, v40
	s_waitcnt vmcnt(7)
	v_lshlrev_b32_e32 v32, 16, v82
	v_mul_f32_e32 v37, v37, v49
	v_mul_f32_e32 v35, v35, v56
	v_mul_f32_e32 v39, v39, v32
	v_and_b32_e32 v32, 0xffff0000, v82
	v_mul_f32_e32 v35, v35, v50
	v_mul_f32_e32 v33, v33, v56
	v_mul_f32_e32 v37, v37, v32
	v_lshlrev_b32_e32 v32, 16, v83
	v_mul_f32_e32 v33, v33, v51
	v_mul_f32_e32 v35, v35, v32
	v_and_b32_e32 v32, 0xffff0000, v83
	v_mul_f32_e32 v41, v33, v32
	v_cvt_pk_bf16_f32 v32, v38, v36
	v_cvt_pk_bf16_f32 v33, v34, v40
	v_cvt_pk_bf16_f32 v34, v39, v37
	v_cvt_pk_bf16_f32 v35, v35, v41
	v_or_b32_e32 v36, 0x140, v58
	v_permlane32_swap_b32_e32 v32, v34
	v_permlane32_swap_b32_e32 v33, v35
	global_store_dwordx4 v36, v[32:35], s[4:5] offset:32
	global_load_dwordx2 v[40:41], v59, s[4:5] offset:448
	global_load_dwordx2 v[42:43], v59, s[4:5] offset:464
	global_load_dwordx2 v[44:45], v59, s[4:5] offset:480
	global_load_dwordx2 v[46:47], v59, s[4:5] offset:496
	ds_read_b128 v[32:35], v57 offset:768
	ds_read_b128 v[36:39], v57 offset:800
	v_mul_f32_e32 v30, v30, v56
	v_mul_f32_e32 v28, v28, v56
	v_mul_f32_e32 v26, v26, v56
	s_waitcnt lgkmcnt(1)
	v_mul_f32_e32 v30, v30, v32
	s_waitcnt vmcnt(9)
	v_lshlrev_b32_e32 v32, 16, v60
	v_mul_f32_e32 v28, v28, v33
	v_mul_f32_e32 v30, v30, v32
	v_and_b32_e32 v32, 0xffff0000, v60
	v_mul_f32_e32 v26, v26, v34
	v_mul_f32_e32 v24, v24, v56
	v_mul_f32_e32 v28, v28, v32
	v_lshlrev_b32_e32 v32, 16, v61
	v_mul_f32_e32 v31, v31, v56
	v_mul_f32_e32 v24, v24, v35
	v_mul_f32_e32 v26, v26, v32
	v_and_b32_e32 v32, 0xffff0000, v61
	s_waitcnt lgkmcnt(0)
	v_mul_f32_e32 v31, v31, v36
	v_mul_f32_e32 v29, v29, v56
	v_mul_f32_e32 v32, v24, v32
	s_waitcnt vmcnt(8)
	v_lshlrev_b32_e32 v24, 16, v62
	v_mul_f32_e32 v29, v29, v37
	v_mul_f32_e32 v27, v27, v56
	v_mul_f32_e32 v31, v31, v24
	v_and_b32_e32 v24, 0xffff0000, v62
	v_mul_f32_e32 v27, v27, v38
	v_mul_f32_e32 v25, v25, v56
	v_mul_f32_e32 v29, v29, v24
	v_lshlrev_b32_e32 v24, 16, v63
	v_mul_f32_e32 v25, v25, v39
	v_mul_f32_e32 v27, v27, v24
	v_and_b32_e32 v24, 0xffff0000, v63
	v_mul_f32_e32 v33, v25, v24
	v_cvt_pk_bf16_f32 v24, v30, v28
	v_cvt_pk_bf16_f32 v25, v26, v32
	v_cvt_pk_bf16_f32 v26, v31, v29
	v_cvt_pk_bf16_f32 v27, v27, v33
	ds_read_b128 v[28:31], v57 offset:832
	ds_read_b128 v[32:35], v57 offset:864
	v_permlane32_swap_b32_e32 v24, v26
	v_permlane32_swap_b32_e32 v25, v27
	v_mul_f32_e32 v22, v22, v56
	global_store_dwordx4 v58, v[24:27], s[4:5] offset:384
	s_waitcnt lgkmcnt(1)
	v_mul_f32_e32 v22, v22, v28
	v_mul_f32_e32 v20, v20, v56
	s_waitcnt vmcnt(8)
	v_lshlrev_b32_e32 v24, 16, v64
	v_mul_f32_e32 v20, v20, v29
	v_mul_f32_e32 v18, v18, v56
	v_mul_f32_e32 v22, v22, v24
	v_and_b32_e32 v24, 0xffff0000, v64
	v_mul_f32_e32 v18, v18, v30
	v_mul_f32_e32 v16, v16, v56
	v_mul_f32_e32 v20, v20, v24
	v_lshlrev_b32_e32 v24, 16, v65
	v_mul_f32_e32 v23, v23, v56
	v_mul_f32_e32 v16, v16, v31
	v_mul_f32_e32 v18, v18, v24
	v_and_b32_e32 v24, 0xffff0000, v65
	s_waitcnt lgkmcnt(0)
	v_mul_f32_e32 v23, v23, v32
	v_mul_f32_e32 v21, v21, v56
	v_mul_f32_e32 v24, v16, v24
	s_waitcnt vmcnt(7)
	v_lshlrev_b32_e32 v16, 16, v66
	v_mul_f32_e32 v21, v21, v33
	v_mul_f32_e32 v19, v19, v56
	v_mul_f32_e32 v23, v23, v16
	v_and_b32_e32 v16, 0xffff0000, v66
	v_mul_f32_e32 v19, v19, v34
	v_mul_f32_e32 v17, v17, v56
	v_mul_f32_e32 v21, v21, v16
	v_lshlrev_b32_e32 v16, 16, v67
	v_mul_f32_e32 v17, v17, v35
	v_mul_f32_e32 v19, v19, v16
	v_and_b32_e32 v16, 0xffff0000, v67
	v_mul_f32_e32 v25, v17, v16
	v_cvt_pk_bf16_f32 v16, v22, v20
	v_cvt_pk_bf16_f32 v17, v18, v24
	v_cvt_pk_bf16_f32 v18, v23, v21
	v_cvt_pk_bf16_f32 v19, v19, v25
	v_or_b32_e32 v20, 0x180, v58
	v_permlane32_swap_b32_e32 v16, v18
	v_permlane32_swap_b32_e32 v17, v19
	global_store_dwordx4 v20, v[16:19], s[4:5] offset:32
	ds_read_b128 v[16:19], v57 offset:896
	ds_read_b128 v[20:23], v57 offset:928
	v_mul_f32_e32 v14, v14, v56
	v_mul_f32_e32 v12, v12, v56
	v_mul_f32_e32 v10, v10, v56
	s_waitcnt lgkmcnt(1)
	v_mul_f32_e32 v14, v14, v16
	s_waitcnt vmcnt(5)
	v_lshlrev_b32_e32 v16, 16, v40
	v_mul_f32_e32 v12, v12, v17
	v_mul_f32_e32 v14, v14, v16
	v_and_b32_e32 v16, 0xffff0000, v40
	v_mul_f32_e32 v10, v10, v18
	v_mul_f32_e32 v8, v8, v56
	v_mul_f32_e32 v12, v12, v16
	v_lshlrev_b32_e32 v16, 16, v41
	v_mul_f32_e32 v15, v15, v56
	v_mul_f32_e32 v8, v8, v19
	v_mul_f32_e32 v10, v10, v16
	v_and_b32_e32 v16, 0xffff0000, v41
	s_waitcnt lgkmcnt(0)
	v_mul_f32_e32 v15, v15, v20
	v_mul_f32_e32 v13, v13, v56
	v_mul_f32_e32 v16, v8, v16
	s_waitcnt vmcnt(4)
	v_lshlrev_b32_e32 v8, 16, v42
	v_mul_f32_e32 v13, v13, v21
	v_mul_f32_e32 v11, v11, v56
	v_mul_f32_e32 v15, v15, v8
	v_and_b32_e32 v8, 0xffff0000, v42
	v_mul_f32_e32 v11, v11, v22
	v_mul_f32_e32 v9, v9, v56
	v_mul_f32_e32 v13, v13, v8
	v_lshlrev_b32_e32 v8, 16, v43
	v_mul_f32_e32 v9, v9, v23
	v_mul_f32_e32 v11, v11, v8
	v_and_b32_e32 v8, 0xffff0000, v43
	v_mul_f32_e32 v17, v9, v8
	v_cvt_pk_bf16_f32 v8, v14, v12
	v_cvt_pk_bf16_f32 v9, v10, v16
	v_cvt_pk_bf16_f32 v10, v15, v13
	v_cvt_pk_bf16_f32 v11, v11, v17
	ds_read_b128 v[12:15], v57 offset:960
	ds_read_b128 v[16:19], v57 offset:992
	v_permlane32_swap_b32_e32 v8, v10
	v_permlane32_swap_b32_e32 v9, v11
	v_mul_f32_e32 v6, v6, v56
	global_store_dwordx4 v58, v[8:11], s[4:5] offset:448
	s_waitcnt lgkmcnt(1)
	v_mul_f32_e32 v6, v6, v12
	v_mul_f32_e32 v4, v4, v56
	s_waitcnt vmcnt(4)
	v_lshlrev_b32_e32 v8, 16, v44
	v_mul_f32_e32 v4, v4, v13
	v_mul_f32_e32 v2, v2, v56
	v_mul_f32_e32 v6, v6, v8
	v_and_b32_e32 v8, 0xffff0000, v44
	v_mul_f32_e32 v2, v2, v14
	v_mul_f32_e32 v0, v0, v56
	v_mul_f32_e32 v4, v4, v8
	v_lshlrev_b32_e32 v8, 16, v45
	v_mul_f32_e32 v7, v7, v56
	v_mul_f32_e32 v0, v0, v15
	v_mul_f32_e32 v2, v2, v8
	v_and_b32_e32 v8, 0xffff0000, v45
	s_waitcnt lgkmcnt(0)
	v_mul_f32_e32 v7, v7, v16
	v_mul_f32_e32 v5, v5, v56
	v_mul_f32_e32 v8, v0, v8
	s_waitcnt vmcnt(3)
	v_lshlrev_b32_e32 v0, 16, v46
	v_mul_f32_e32 v5, v5, v17
	v_mul_f32_e32 v3, v3, v56
	v_mul_f32_e32 v7, v7, v0
	v_and_b32_e32 v0, 0xffff0000, v46
	v_mul_f32_e32 v3, v3, v18
	v_mul_f32_e32 v1, v1, v56
	v_mul_f32_e32 v5, v5, v0
	v_lshlrev_b32_e32 v0, 16, v47
	v_mul_f32_e32 v1, v1, v19
	v_mul_f32_e32 v3, v3, v0
	v_and_b32_e32 v0, 0xffff0000, v47
	v_mul_f32_e32 v9, v1, v0
	v_cvt_pk_bf16_f32 v0, v6, v4
	v_cvt_pk_bf16_f32 v1, v2, v8
	v_cvt_pk_bf16_f32 v2, v7, v5
	v_cvt_pk_bf16_f32 v3, v3, v9
	v_readlane_b32 s2, v255, 38
	v_permlane32_swap_b32_e32 v0, v2
	v_permlane32_swap_b32_e32 v1, v3
	v_or_b32_e32 v4, 0x1c0, v58
	s_cmp_lg_u32 s10, s2
	s_mov_b32 s2, s10
	global_store_dwordx4 v4, v[0:3], s[4:5] offset:32
	s_cbranch_scc0 .LBB0_541

.Lstg_b6:
	s_add_i32 s6, s88, -1
	s_cmp_ge_u32 s6, s89
	s_cselect_b64 s[82:83], -1, 0
	s_mov_b64 s[4:5], -1
	s_and_b64 vcc, exec, s[82:83]
	s_cbranch_vccz .LBB0_524
	v_mov_b64_e32 v[144:145], s[0:1]
	flat_load_dword v146, v[144:145] sc0 sc1
	v_mov_b64_e32 v[144:145], s[74:75]
	flat_load_dword v144, v[144:145] sc0 sc1
	s_waitcnt vmcnt(0) lgkmcnt(0)
	v_readfirstlane_b32 s4, v146
	v_readfirstlane_b32 s5, v144
	s_nop 1
	s_nop 3
	s_mov_b32 m0, s2
	s_nop 0
	global_load_lds_dwordx4 v170, s[4:5]
	s_nop 3
	s_mov_b32 m0, s91
	s_nop 0
	global_load_lds_dwordx4 v172, s[4:5]
	s_mov_b64 s[4:5], 0

.Lstg_b7:
	s_cmp_gt_u32 s88, s89
	s_cbranch_scc1 .LBB0_533
	s_cmp_ge_u32 s88, s89
	s_mov_b64 s[4:5], -1
	s_cbranch_scc0 .LBB0_531
	v_mov_b64_e32 v[194:195], s[0:1]
	flat_load_dword v196, v[194:195] sc0 sc1
	v_mov_b64_e32 v[194:195], s[74:75]
	flat_load_dword v194, v[194:195] sc0 sc1
	s_waitcnt vmcnt(0) lgkmcnt(0)
	v_readfirstlane_b32 s4, v196
	v_readfirstlane_b32 s5, v194
	s_nop 1
	s_nop 3
	s_mov_b32 m0, s2
	s_nop 0
	global_load_lds_dwordx4 v170, s[4:5]
	s_nop 3
	s_mov_b32 m0, s91
	s_nop 0
	global_load_lds_dwordx4 v172, s[4:5]
	s_mov_b64 s[4:5], 0

.LBB0_533:
	s_mov_b64 s[4:5], -1
	s_and_b64 vcc, exec, s[82:83]
	s_cbranch_vccz .LBB0_535
	v_mov_b64_e32 v[194:195], s[70:71]
	flat_load_dword v196, v[194:195] sc0 sc1
	v_mov_b64_e32 v[194:195], s[76:77]
	flat_load_dword v194, v[194:195] sc0 sc1
	s_waitcnt vmcnt(0) lgkmcnt(0)
	v_readfirstlane_b32 s4, v196
	v_readfirstlane_b32 s5, v194
	s_nop 1
	s_nop 3
	s_mov_b32 m0, s81
	s_nop 0
	global_load_lds_dwordx4 v162, s[4:5]
	s_nop 3
	s_add_i32 m0, s78, 0xffffff80
	s_nop 0
	global_load_lds_dwordx4 v162, s[4:5] offset:128
	s_add_i32 m0, s69, 0xffffff00
	s_nop 0
	global_load_lds_dwordx4 v162, s[4:5] offset:256
	s_add_i32 m0, s68, 0xfffffe80
	s_nop 0
	global_load_lds_dwordx4 v162, s[4:5] offset:384
	s_mov_b64 s[4:5], 0

.Lstg_b14:
	s_add_i32 s8, s3, -1
	s_cmp_ge_u32 s8, s75
	s_cselect_b64 s[96:97], -1, 0
	s_mov_b64 s[6:7], -1
	s_and_b64 vcc, exec, s[96:97]
	s_cbranch_vccz .LBB0_561
	v_mov_b64_e32 v[144:145], s[80:81]
	flat_load_dword v146, v[144:145] sc0 sc1
	v_mov_b64_e32 v[144:145], s[72:73]
	flat_load_dword v144, v[144:145] sc0 sc1
	s_waitcnt vmcnt(0) lgkmcnt(0)
	v_readfirstlane_b32 s6, v146
	v_readfirstlane_b32 s7, v144
	s_nop 1
	s_nop 3
	s_mov_b32 m0, s83
	s_nop 0
	global_load_lds_dwordx4 v160, s[6:7]
	s_nop 3
	s_mov_b32 m0, s78
	s_nop 0
	global_load_lds_dwordx4 v170, s[6:7]
	s_mov_b64 s[6:7], 0

.Lstg_b15:
	s_cmp_gt_u32 s3, s75
	s_cbranch_scc1 .LBB0_572
	s_cmp_ge_u32 s3, s75
	s_mov_b64 s[6:7], -1
	s_cbranch_scc0 .LBB0_570
	v_mov_b64_e32 v[148:149], s[80:81]
	flat_load_dword v144, v[148:149] sc0 sc1
	v_mov_b64_e32 v[148:149], s[72:73]
	flat_load_dword v147, v[148:149] sc0 sc1
	s_waitcnt vmcnt(0) lgkmcnt(0)
	v_readfirstlane_b32 s6, v144
	v_readfirstlane_b32 s7, v147
	s_nop 1
	s_nop 3
	s_mov_b32 m0, s83
	s_nop 0
	global_load_lds_dwordx4 v160, s[6:7]
	s_nop 3
	s_mov_b32 m0, s78
	s_nop 0
	global_load_lds_dwordx4 v170, s[6:7]
	s_mov_b64 s[6:7], 0

.LBB0_572:
	s_mov_b64 s[6:7], -1
	s_and_b64 vcc, exec, s[96:97]
	s_cbranch_vccz .LBB0_574
	v_mov_b64_e32 v[148:149], s[0:1]
	flat_load_dword v144, v[148:149] sc0 sc1
	v_mov_b64_e32 v[148:149], s[70:71]
	flat_load_dword v147, v[148:149] sc0 sc1
	s_waitcnt vmcnt(0) lgkmcnt(0)
	v_readfirstlane_b32 s6, v144
	v_readfirstlane_b32 s7, v147
	s_nop 1
	s_nop 3
	s_mov_b32 m0, s93
	s_nop 0
	global_load_lds_dwordx4 v162, s[6:7]
	s_nop 3
	s_add_i32 m0, s2, 0xffffff80
	s_nop 0
	global_load_lds_dwordx4 v162, s[6:7] offset:128
	s_add_i32 m0, s69, 0xffffff00
	s_nop 0
	global_load_lds_dwordx4 v162, s[6:7] offset:256
	s_add_i32 m0, s68, 0xfffffe80
	s_nop 0
	global_load_lds_dwordx4 v162, s[6:7] offset:384
	s_mov_b64 s[6:7], 0

.Lstg_b16:
	v_mov_b64_e32 v[146:147], s[0:1]
	flat_load_dword v148, v[146:147] sc0 sc1
	v_mov_b64_e32 v[146:147], s[70:71]
	flat_load_dword v146, v[146:147] sc0 sc1
	s_waitcnt vmcnt(0) lgkmcnt(0)
	v_readfirstlane_b32 s4, v148
	v_readfirstlane_b32 s5, v146
	s_nop 1
	s_nop 3
	s_mov_b32 m0, s93
	s_nop 0
	global_load_lds_dwordx4 v162, s[4:5]
	s_nop 3
	s_add_i32 m0, s2, 0xffffff80
	s_nop 0
	global_load_lds_dwordx4 v162, s[4:5] offset:128
	s_add_i32 m0, s69, 0xffffff00
	s_nop 0
	global_load_lds_dwordx4 v162, s[4:5] offset:256
	s_add_i32 m0, s68, 0xfffffe80
	s_nop 0
	global_load_lds_dwordx4 v162, s[4:5] offset:384
	v_cmp_gt_f32_e32 vcc, 1.0, v160
	s_cbranch_vccz .LBB0_584
	v_pk_mul_f32 v[126:127], v[126:127], v[160:161] op_sel_hi:[1,0]
	v_pk_mul_f32 v[124:125], v[124:125], v[160:161] op_sel_hi:[1,0]
	v_pk_mul_f32 v[122:123], v[122:123], v[160:161] op_sel_hi:[1,0]
	v_pk_mul_f32 v[120:121], v[120:121], v[160:161] op_sel_hi:[1,0]
	v_pk_mul_f32 v[118:119], v[118:119], v[160:161] op_sel_hi:[1,0]
	v_pk_mul_f32 v[116:117], v[116:117], v[160:161] op_sel_hi:[1,0]
	v_pk_mul_f32 v[114:115], v[114:115], v[160:161] op_sel_hi:[1,0]
	v_pk_mul_f32 v[112:113], v[112:113], v[160:161] op_sel_hi:[1,0]
	v_pk_mul_f32 v[94:95], v[94:95], v[160:161] op_sel_hi:[1,0]
	v_pk_mul_f32 v[92:93], v[92:93], v[160:161] op_sel_hi:[1,0]
	v_pk_mul_f32 v[90:91], v[90:91], v[160:161] op_sel_hi:[1,0]
	v_pk_mul_f32 v[88:89], v[88:89], v[160:161] op_sel_hi:[1,0]
	v_pk_mul_f32 v[86:87], v[86:87], v[160:161] op_sel_hi:[1,0]
	v_pk_mul_f32 v[84:85], v[84:85], v[160:161] op_sel_hi:[1,0]
	v_pk_mul_f32 v[82:83], v[82:83], v[160:161] op_sel_hi:[1,0]
	v_pk_mul_f32 v[80:81], v[80:81], v[160:161] op_sel_hi:[1,0]
	v_pk_mul_f32 v[110:111], v[110:111], v[160:161] op_sel_hi:[1,0]
	v_pk_mul_f32 v[108:109], v[108:109], v[160:161] op_sel_hi:[1,0]
	v_pk_mul_f32 v[106:107], v[106:107], v[160:161] op_sel_hi:[1,0]
	v_pk_mul_f32 v[104:105], v[104:105], v[160:161] op_sel_hi:[1,0]
	v_pk_mul_f32 v[102:103], v[102:103], v[160:161] op_sel_hi:[1,0]
	v_pk_mul_f32 v[100:101], v[100:101], v[160:161] op_sel_hi:[1,0]
	v_pk_mul_f32 v[98:99], v[98:99], v[160:161] op_sel_hi:[1,0]
	v_pk_mul_f32 v[96:97], v[96:97], v[160:161] op_sel_hi:[1,0]
	v_pk_mul_f32 v[78:79], v[78:79], v[160:161] op_sel_hi:[1,0]
	v_pk_mul_f32 v[76:77], v[76:77], v[160:161] op_sel_hi:[1,0]
	v_pk_mul_f32 v[74:75], v[74:75], v[160:161] op_sel_hi:[1,0]
	v_pk_mul_f32 v[72:73], v[72:73], v[160:161] op_sel_hi:[1,0]
	v_pk_mul_f32 v[70:71], v[70:71], v[160:161] op_sel_hi:[1,0]
	v_pk_mul_f32 v[68:69], v[68:69], v[160:161] op_sel_hi:[1,0]
	v_pk_mul_f32 v[66:67], v[66:67], v[160:161] op_sel_hi:[1,0]
	v_pk_mul_f32 v[64:65], v[64:65], v[160:161] op_sel_hi:[1,0]
	v_pk_mul_f32 v[62:63], v[62:63], v[160:161] op_sel_hi:[1,0]
	v_pk_mul_f32 v[60:61], v[60:61], v[160:161] op_sel_hi:[1,0]
	v_pk_mul_f32 v[58:59], v[58:59], v[160:161] op_sel_hi:[1,0]
	v_pk_mul_f32 v[56:57], v[56:57], v[160:161] op_sel_hi:[1,0]
	v_pk_mul_f32 v[54:55], v[54:55], v[160:161] op_sel_hi:[1,0]
	v_pk_mul_f32 v[52:53], v[52:53], v[160:161] op_sel_hi:[1,0]
	v_pk_mul_f32 v[50:51], v[50:51], v[160:161] op_sel_hi:[1,0]
	v_pk_mul_f32 v[48:49], v[48:49], v[160:161] op_sel_hi:[1,0]
	v_pk_mul_f32 v[46:47], v[46:47], v[160:161] op_sel_hi:[1,0]
	v_pk_mul_f32 v[44:45], v[44:45], v[160:161] op_sel_hi:[1,0]
	v_pk_mul_f32 v[42:43], v[42:43], v[160:161] op_sel_hi:[1,0]
	v_pk_mul_f32 v[40:41], v[40:41], v[160:161] op_sel_hi:[1,0]
	v_pk_mul_f32 v[38:39], v[38:39], v[160:161] op_sel_hi:[1,0]
	v_pk_mul_f32 v[36:37], v[36:37], v[160:161] op_sel_hi:[1,0]
	v_pk_mul_f32 v[34:35], v[34:35], v[160:161] op_sel_hi:[1,0]
	v_pk_mul_f32 v[32:33], v[32:33], v[160:161] op_sel_hi:[1,0]
	v_pk_mul_f32 v[30:31], v[30:31], v[160:161] op_sel_hi:[1,0]
	v_pk_mul_f32 v[28:29], v[28:29], v[160:161] op_sel_hi:[1,0]
	v_pk_mul_f32 v[26:27], v[26:27], v[160:161] op_sel_hi:[1,0]
	v_pk_mul_f32 v[24:25], v[24:25], v[160:161] op_sel_hi:[1,0]
	v_pk_mul_f32 v[22:23], v[22:23], v[160:161] op_sel_hi:[1,0]
	v_pk_mul_f32 v[20:21], v[20:21], v[160:161] op_sel_hi:[1,0]
	v_pk_mul_f32 v[18:19], v[18:19], v[160:161] op_sel_hi:[1,0]
	v_pk_mul_f32 v[16:17], v[16:17], v[160:161] op_sel_hi:[1,0]
	v_pk_mul_f32 v[14:15], v[14:15], v[160:161] op_sel_hi:[1,0]
	v_pk_mul_f32 v[12:13], v[12:13], v[160:161] op_sel_hi:[1,0]
	v_pk_mul_f32 v[10:11], v[10:11], v[160:161] op_sel_hi:[1,0]
	v_pk_mul_f32 v[8:9], v[8:9], v[160:161] op_sel_hi:[1,0]
	v_pk_mul_f32 v[6:7], v[6:7], v[160:161] op_sel_hi:[1,0]
	v_pk_mul_f32 v[4:5], v[4:5], v[160:161] op_sel_hi:[1,0]
	v_pk_mul_f32 v[2:3], v[2:3], v[160:161] op_sel_hi:[1,0]
	v_pk_mul_f32 v[0:1], v[0:1], v[160:161] op_sel_hi:[1,0]

.Lstg_b22:
	s_add_i32 s8, s85, -1
	s_cmp_ge_u32 s8, s75
	s_cselect_b64 s[66:67], -1, 0
	s_mov_b64 s[6:7], -1
	s_and_b64 vcc, exec, s[66:67]
	s_cbranch_vccz .LBB0_593
	v_mov_b64_e32 v[144:145], s[80:81]
	flat_load_dword v146, v[144:145] sc0 sc1
	v_mov_b64_e32 v[144:145], s[72:73]
	flat_load_dword v144, v[144:145] sc0 sc1
	s_waitcnt vmcnt(0) lgkmcnt(0)
	v_readfirstlane_b32 s6, v146
	v_readfirstlane_b32 s7, v144
	s_nop 1
	s_nop 3
	s_mov_b32 m0, s78
	s_nop 0
	global_load_lds_dwordx4 v160, s[6:7]
	s_nop 3
	s_mov_b32 m0, s93
	s_nop 0
	global_load_lds_dwordx4 v170, s[6:7]
	s_mov_b64 s[6:7], 0

.Lstg_b23:
	s_cmp_gt_u32 s85, s75
	s_cbranch_scc1 .LBB0_604
	s_cmp_ge_u32 s85, s75
	s_mov_b64 s[6:7], -1
	s_cbranch_scc0 .LBB0_602
	v_mov_b64_e32 v[148:149], s[80:81]
	flat_load_dword v144, v[148:149] sc0 sc1
	v_mov_b64_e32 v[148:149], s[72:73]
	flat_load_dword v147, v[148:149] sc0 sc1
	s_waitcnt vmcnt(0) lgkmcnt(0)
	v_readfirstlane_b32 s6, v144
	v_readfirstlane_b32 s7, v147
	s_nop 1
	s_nop 3
	s_mov_b32 m0, s78
	s_nop 0
	global_load_lds_dwordx4 v160, s[6:7]
	s_nop 3
	s_mov_b32 m0, s93
	s_nop 0
	global_load_lds_dwordx4 v170, s[6:7]
	s_mov_b64 s[6:7], 0

.LBB0_604:
	s_mov_b64 s[6:7], -1
	s_and_b64 vcc, exec, s[66:67]
	s_cbranch_vccz .LBB0_606
	v_mov_b64_e32 v[148:149], s[0:1]
	flat_load_dword v144, v[148:149] sc0 sc1
	v_mov_b64_e32 v[148:149], s[70:71]
	flat_load_dword v147, v[148:149] sc0 sc1
	s_waitcnt vmcnt(0) lgkmcnt(0)
	v_readfirstlane_b32 s6, v144
	v_readfirstlane_b32 s7, v147
	s_nop 1
	s_nop 3
	s_mov_b32 m0, s3
	s_nop 0
	global_load_lds_dwordx4 v162, s[6:7]
	s_nop 3
	s_add_i32 m0, s69, 0xffffff80
	s_nop 0
	global_load_lds_dwordx4 v162, s[6:7] offset:128
	s_add_i32 m0, s68, 0xffffff00
	s_nop 0
	global_load_lds_dwordx4 v162, s[6:7] offset:256
	s_add_i32 m0, s2, 0xfffffe80
	s_nop 0
	global_load_lds_dwordx4 v162, s[6:7] offset:384
	s_mov_b64 s[6:7], 0

.Lstg_b24:
	v_mov_b64_e32 v[146:147], s[0:1]
	flat_load_dword v148, v[146:147] sc0 sc1
	v_mov_b64_e32 v[146:147], s[70:71]
	flat_load_dword v146, v[146:147] sc0 sc1
	s_waitcnt vmcnt(0) lgkmcnt(0)
	v_readfirstlane_b32 s4, v148
	v_readfirstlane_b32 s5, v146
	s_nop 1
	s_nop 3
	s_mov_b32 m0, s3
	s_nop 0
	global_load_lds_dwordx4 v162, s[4:5]
	s_nop 3
	s_add_i32 m0, s69, 0xffffff80
	s_nop 0
	global_load_lds_dwordx4 v162, s[4:5] offset:128
	s_add_i32 m0, s68, 0xffffff00
	s_nop 0
	global_load_lds_dwordx4 v162, s[4:5] offset:256
	s_add_i32 m0, s2, 0xfffffe80
	s_nop 0
	global_load_lds_dwordx4 v162, s[4:5] offset:384
	v_cmp_gt_f32_e32 vcc, 1.0, v160
	s_cbranch_vccz .LBB0_551
	v_pk_mul_f32 v[126:127], v[126:127], v[160:161] op_sel_hi:[1,0]
	v_pk_mul_f32 v[124:125], v[124:125], v[160:161] op_sel_hi:[1,0]
	v_pk_mul_f32 v[122:123], v[122:123], v[160:161] op_sel_hi:[1,0]
	v_pk_mul_f32 v[120:121], v[120:121], v[160:161] op_sel_hi:[1,0]
	v_pk_mul_f32 v[118:119], v[118:119], v[160:161] op_sel_hi:[1,0]
	v_pk_mul_f32 v[116:117], v[116:117], v[160:161] op_sel_hi:[1,0]
	v_pk_mul_f32 v[114:115], v[114:115], v[160:161] op_sel_hi:[1,0]
	v_pk_mul_f32 v[112:113], v[112:113], v[160:161] op_sel_hi:[1,0]
	v_pk_mul_f32 v[110:111], v[110:111], v[160:161] op_sel_hi:[1,0]
	v_pk_mul_f32 v[108:109], v[108:109], v[160:161] op_sel_hi:[1,0]
	v_pk_mul_f32 v[106:107], v[106:107], v[160:161] op_sel_hi:[1,0]
	v_pk_mul_f32 v[104:105], v[104:105], v[160:161] op_sel_hi:[1,0]
	v_pk_mul_f32 v[102:103], v[102:103], v[160:161] op_sel_hi:[1,0]
	v_pk_mul_f32 v[100:101], v[100:101], v[160:161] op_sel_hi:[1,0]
	v_pk_mul_f32 v[98:99], v[98:99], v[160:161] op_sel_hi:[1,0]
	v_pk_mul_f32 v[96:97], v[96:97], v[160:161] op_sel_hi:[1,0]
	v_pk_mul_f32 v[94:95], v[94:95], v[160:161] op_sel_hi:[1,0]
	v_pk_mul_f32 v[92:93], v[92:93], v[160:161] op_sel_hi:[1,0]
	v_pk_mul_f32 v[90:91], v[90:91], v[160:161] op_sel_hi:[1,0]
	v_pk_mul_f32 v[88:89], v[88:89], v[160:161] op_sel_hi:[1,0]
	v_pk_mul_f32 v[86:87], v[86:87], v[160:161] op_sel_hi:[1,0]
	v_pk_mul_f32 v[84:85], v[84:85], v[160:161] op_sel_hi:[1,0]
	v_pk_mul_f32 v[82:83], v[82:83], v[160:161] op_sel_hi:[1,0]
	v_pk_mul_f32 v[80:81], v[80:81], v[160:161] op_sel_hi:[1,0]
	v_pk_mul_f32 v[78:79], v[78:79], v[160:161] op_sel_hi:[1,0]
	v_pk_mul_f32 v[76:77], v[76:77], v[160:161] op_sel_hi:[1,0]
	v_pk_mul_f32 v[74:75], v[74:75], v[160:161] op_sel_hi:[1,0]
	v_pk_mul_f32 v[72:73], v[72:73], v[160:161] op_sel_hi:[1,0]
	v_pk_mul_f32 v[70:71], v[70:71], v[160:161] op_sel_hi:[1,0]
	v_pk_mul_f32 v[68:69], v[68:69], v[160:161] op_sel_hi:[1,0]
	v_pk_mul_f32 v[66:67], v[66:67], v[160:161] op_sel_hi:[1,0]
	v_pk_mul_f32 v[64:65], v[64:65], v[160:161] op_sel_hi:[1,0]
	v_pk_mul_f32 v[62:63], v[62:63], v[160:161] op_sel_hi:[1,0]
	v_pk_mul_f32 v[60:61], v[60:61], v[160:161] op_sel_hi:[1,0]
	v_pk_mul_f32 v[58:59], v[58:59], v[160:161] op_sel_hi:[1,0]
	v_pk_mul_f32 v[56:57], v[56:57], v[160:161] op_sel_hi:[1,0]
	v_pk_mul_f32 v[54:55], v[54:55], v[160:161] op_sel_hi:[1,0]
	v_pk_mul_f32 v[52:53], v[52:53], v[160:161] op_sel_hi:[1,0]
	v_pk_mul_f32 v[50:51], v[50:51], v[160:161] op_sel_hi:[1,0]
	v_pk_mul_f32 v[48:49], v[48:49], v[160:161] op_sel_hi:[1,0]
	v_pk_mul_f32 v[46:47], v[46:47], v[160:161] op_sel_hi:[1,0]
	v_pk_mul_f32 v[44:45], v[44:45], v[160:161] op_sel_hi:[1,0]
	v_pk_mul_f32 v[42:43], v[42:43], v[160:161] op_sel_hi:[1,0]
	v_pk_mul_f32 v[40:41], v[40:41], v[160:161] op_sel_hi:[1,0]
	v_pk_mul_f32 v[38:39], v[38:39], v[160:161] op_sel_hi:[1,0]
	v_pk_mul_f32 v[36:37], v[36:37], v[160:161] op_sel_hi:[1,0]
	v_pk_mul_f32 v[34:35], v[34:35], v[160:161] op_sel_hi:[1,0]
	v_pk_mul_f32 v[32:33], v[32:33], v[160:161] op_sel_hi:[1,0]
	v_pk_mul_f32 v[30:31], v[30:31], v[160:161] op_sel_hi:[1,0]
	v_pk_mul_f32 v[28:29], v[28:29], v[160:161] op_sel_hi:[1,0]
	v_pk_mul_f32 v[26:27], v[26:27], v[160:161] op_sel_hi:[1,0]
	v_pk_mul_f32 v[24:25], v[24:25], v[160:161] op_sel_hi:[1,0]
	v_pk_mul_f32 v[22:23], v[22:23], v[160:161] op_sel_hi:[1,0]
	v_pk_mul_f32 v[20:21], v[20:21], v[160:161] op_sel_hi:[1,0]
	v_pk_mul_f32 v[18:19], v[18:19], v[160:161] op_sel_hi:[1,0]
	v_pk_mul_f32 v[16:17], v[16:17], v[160:161] op_sel_hi:[1,0]
	v_pk_mul_f32 v[14:15], v[14:15], v[160:161] op_sel_hi:[1,0]
	v_pk_mul_f32 v[12:13], v[12:13], v[160:161] op_sel_hi:[1,0]
	v_pk_mul_f32 v[10:11], v[10:11], v[160:161] op_sel_hi:[1,0]
	v_pk_mul_f32 v[8:9], v[8:9], v[160:161] op_sel_hi:[1,0]
	v_pk_mul_f32 v[6:7], v[6:7], v[160:161] op_sel_hi:[1,0]
	v_pk_mul_f32 v[4:5], v[4:5], v[160:161] op_sel_hi:[1,0]
	v_pk_mul_f32 v[2:3], v[2:3], v[160:161] op_sel_hi:[1,0]
	v_pk_mul_f32 v[0:1], v[0:1], v[160:161] op_sel_hi:[1,0]
	s_branch .LBB0_551
